# SwiGLU epilogues (dense + MoE FFN-up) rewritten with packed f32 mul/add; same per-element operation order
# speedup vs baseline: 1.0051x; 1.0051x over previous
; DI unsigned pk4_fp8(float a, float b, float c, float d) { int w = __builtin_amdgcn_cvt_pk_fp8_f32(sat8(a), sat8(b), 0, false); w = __builtin_amdgcn_cvt_pk_fp8_f32(sat8(c), sat8(d), w, true); return (unsigned)w; }
; DI float sig_(float x) { return __builtin_amdgcn_rcpf(1.0f + __builtin_amdgcn_exp2f(-1.4426950408889634f * x)); }
;     DI void operator()(const f32x4 (&acc)[2][2][4][2], const Unit& u, int wr, int wc, int fr, int fq) const {
;         int row0 = u.pm * BM + wr * 64 + fr; asm volatile("" : "+v"(row0));
;         int coff = wc * 32 + 8 * fq; asm volatile("" : "+v"(coff));
;         unsigned char* base = Hm + u.pn * HALF + coff;
; #pragma unroll
;         for (int ai = 0; ai < 2; ++ai)
; #pragma unroll
;             for (int m = 0; m < 4; ++m) { unsigned char* rowp = base + (size_t)(row0 + ai * HALF + m * 16) * ld;
;                 float o[8];
; #pragma unroll
;                 for (int n = 0; n < 2; ++n)
; #pragma unroll
;                     for (int e = 0; e < 4; ++e) { const float a = acc[ai][0][m][n][e], b = acc[ai][1][m][n][e]; o[n * 4 + e] = a * sig_(a) * (b * H_SC); }
;                 *(u32x2*)rowp = (u32x2){pk4_fp8(o[0], o[1], o[2], o[3]), pk4_fp8(o[4], o[5], o[6], o[7])}; }
.LBB0_703:
	s_lshl_b32 s13, s66, 7
	s_ashr_i32 s17, s13, 31
	v_lshl_add_u32 v148, s22, 8, v140
	v_mov_b32_e32 v134, v141
	s_add_u32 s24, s53, s13
	s_addc_u32 s25, s54, s17
	v_ashrrev_i32_e32 v135, 31, v134
	s_mov_b32 s98, 0xbfb8aa3b
	s_mov_b32 s100, 1.0
	v_lshl_add_u64 v[134:135], s[24:25], 0, v[134:135]
	s_andn2_b64 vcc, exec, s[4:5]
	s_mov_b64 s[4:5], -1
	v_pk_mul_f32 v[150:151], v[124:125], s[98:99] op_sel_hi:[1,0]
	v_exp_f32_e32 v150, v150
	v_exp_f32_e32 v151, v151
	v_pk_mul_f32 v[120:121], v[120:121], v[132:133] op_sel:[0,1] op_sel_hi:[1,1]
	v_pk_add_f32 v[150:151], v[150:151], s[100:101] op_sel_hi:[1,0]
	v_rcp_f32_e32 v150, v150
	v_rcp_f32_e32 v151, v151
	s_nop 0
	v_pk_mul_f32 v[124:125], v[124:125], v[150:151]
	v_pk_mul_f32 v[124:125], v[124:125], v[120:121]
	v_pk_mul_f32 v[150:151], v[126:127], s[98:99] op_sel_hi:[1,0]
	v_exp_f32_e32 v150, v150
	v_exp_f32_e32 v151, v151
	v_pk_mul_f32 v[122:123], v[122:123], v[132:133] op_sel:[0,1] op_sel_hi:[1,1]
	v_pk_add_f32 v[150:151], v[150:151], s[100:101] op_sel_hi:[1,0]
	v_rcp_f32_e32 v150, v150
	v_rcp_f32_e32 v151, v151
	s_nop 0
	v_pk_mul_f32 v[126:127], v[126:127], v[150:151]
	v_pk_mul_f32 v[126:127], v[126:127], v[122:123]
	v_med3_f32 v124, v124, s65, v147
	v_med3_f32 v125, v125, s65, v147
	v_cvt_pk_fp8_f32 v120, v124, v125
	v_med3_f32 v126, v126, s65, v147
	v_med3_f32 v127, v127, s65, v147
	v_cvt_pk_fp8_f32 v120, v126, v127 op_sel:[0,0,1]
	v_mad_i64_i32 v[122:123], s[24:25], v148, s64, v[134:135]
	v_pk_mul_f32 v[150:151], v[116:117], s[98:99] op_sel_hi:[1,0]
	v_exp_f32_e32 v150, v150
	v_exp_f32_e32 v151, v151
	v_pk_mul_f32 v[112:113], v[112:113], v[132:133] op_sel:[0,1] op_sel_hi:[1,1]
	v_pk_add_f32 v[150:151], v[150:151], s[100:101] op_sel_hi:[1,0]
	v_rcp_f32_e32 v150, v150
	v_rcp_f32_e32 v151, v151
	s_nop 0
	v_pk_mul_f32 v[116:117], v[116:117], v[150:151]
	v_pk_mul_f32 v[116:117], v[116:117], v[112:113]
	v_pk_mul_f32 v[150:151], v[118:119], s[98:99] op_sel_hi:[1,0]
	v_exp_f32_e32 v150, v150
	v_exp_f32_e32 v151, v151
	v_pk_mul_f32 v[114:115], v[114:115], v[132:133] op_sel:[0,1] op_sel_hi:[1,1]
	v_pk_add_f32 v[150:151], v[150:151], s[100:101] op_sel_hi:[1,0]
	v_rcp_f32_e32 v150, v150
	v_rcp_f32_e32 v151, v151
	s_nop 0
	v_pk_mul_f32 v[118:119], v[118:119], v[150:151]
	v_pk_mul_f32 v[118:119], v[118:119], v[114:115]
	v_med3_f32 v116, v116, s65, v147
	v_med3_f32 v117, v117, s65, v147
	v_cvt_pk_fp8_f32 v121, v116, v117
	v_med3_f32 v118, v118, s65, v147
	v_med3_f32 v119, v119, s65, v147
	v_cvt_pk_fp8_f32 v121, v118, v119 op_sel:[0,0,1]
	global_store_dwordx2 v[122:123], v[120:121], off
	v_pk_mul_f32 v[112:113], v[108:109], s[98:99] op_sel_hi:[1,0]
	v_pk_mul_f32 v[114:115], v[110:111], s[98:99] op_sel_hi:[1,0]
	v_exp_f32_e32 v112, v112
	v_exp_f32_e32 v113, v113
	v_exp_f32_e32 v114, v114
	v_exp_f32_e32 v115, v115
	v_pk_add_f32 v[112:113], v[112:113], s[100:101] op_sel_hi:[1,0]
	v_pk_add_f32 v[114:115], v[114:115], s[100:101] op_sel_hi:[1,0]
	v_rcp_f32_e32 v112, v112
	v_rcp_f32_e32 v113, v113
	v_rcp_f32_e32 v114, v114
	v_rcp_f32_e32 v115, v115
	v_pk_mul_f32 v[104:105], v[104:105], v[132:133] op_sel:[0,1] op_sel_hi:[1,1]
	v_pk_mul_f32 v[106:107], v[106:107], v[132:133] op_sel:[0,1] op_sel_hi:[1,1]
	v_pk_mul_f32 v[108:109], v[108:109], v[112:113]
	v_pk_mul_f32 v[110:111], v[110:111], v[114:115]
	v_pk_mul_f32 v[108:109], v[108:109], v[104:105]
	v_pk_mul_f32 v[110:111], v[110:111], v[106:107]
	v_med3_f32 v108, v108, s65, v147
	v_med3_f32 v109, v109, s65, v147
	v_cvt_pk_fp8_f32 v104, v108, v109
	v_med3_f32 v110, v110, s65, v147
	v_med3_f32 v111, v111, s65, v147
	v_cvt_pk_fp8_f32 v104, v110, v111 op_sel:[0,0,1]
	v_add_u32_e32 v106, 0x10, v148
	v_mad_i64_i32 v[106:107], s[24:25], v106, s64, v[134:135]
	v_pk_mul_f32 v[112:113], v[100:101], s[98:99] op_sel_hi:[1,0]
	v_pk_mul_f32 v[114:115], v[102:103], s[98:99] op_sel_hi:[1,0]
	v_exp_f32_e32 v112, v112
	v_exp_f32_e32 v113, v113
	v_exp_f32_e32 v114, v114
	v_exp_f32_e32 v115, v115
	v_pk_add_f32 v[112:113], v[112:113], s[100:101] op_sel_hi:[1,0]
	v_pk_add_f32 v[114:115], v[114:115], s[100:101] op_sel_hi:[1,0]
	v_rcp_f32_e32 v112, v112
	v_rcp_f32_e32 v113, v113
	v_rcp_f32_e32 v114, v114
	v_rcp_f32_e32 v115, v115
	v_pk_mul_f32 v[96:97], v[96:97], v[132:133] op_sel:[0,1] op_sel_hi:[1,1]
	v_pk_mul_f32 v[98:99], v[98:99], v[132:133] op_sel:[0,1] op_sel_hi:[1,1]
	v_pk_mul_f32 v[100:101], v[100:101], v[112:113]
	v_pk_mul_f32 v[102:103], v[102:103], v[114:115]
	v_pk_mul_f32 v[100:101], v[100:101], v[96:97]
	v_pk_mul_f32 v[102:103], v[102:103], v[98:99]
	v_med3_f32 v100, v100, s65, v147
	v_med3_f32 v101, v101, s65, v147
	v_cvt_pk_fp8_f32 v105, v100, v101
	v_med3_f32 v102, v102, s65, v147
	v_med3_f32 v103, v103, s65, v147
	v_cvt_pk_fp8_f32 v105, v102, v103 op_sel:[0,0,1]
	global_store_dwordx2 v[106:107], v[104:105], off
	v_pk_mul_f32 v[112:113], v[92:93], s[98:99] op_sel_hi:[1,0]
	v_pk_mul_f32 v[114:115], v[94:95], s[98:99] op_sel_hi:[1,0]
	v_exp_f32_e32 v112, v112
	v_exp_f32_e32 v113, v113
	v_exp_f32_e32 v114, v114
	v_exp_f32_e32 v115, v115
	v_pk_add_f32 v[112:113], v[112:113], s[100:101] op_sel_hi:[1,0]
	v_pk_add_f32 v[114:115], v[114:115], s[100:101] op_sel_hi:[1,0]
	v_rcp_f32_e32 v112, v112
	v_rcp_f32_e32 v113, v113
	v_rcp_f32_e32 v114, v114
	v_rcp_f32_e32 v115, v115
	v_pk_mul_f32 v[88:89], v[88:89], v[132:133] op_sel:[0,1] op_sel_hi:[1,1]
	v_pk_mul_f32 v[90:91], v[90:91], v[132:133] op_sel:[0,1] op_sel_hi:[1,1]
	v_pk_mul_f32 v[92:93], v[92:93], v[112:113]
	v_pk_mul_f32 v[94:95], v[94:95], v[114:115]
	v_pk_mul_f32 v[92:93], v[92:93], v[88:89]
	v_pk_mul_f32 v[94:95], v[94:95], v[90:91]
	v_med3_f32 v92, v92, s65, v147
	v_med3_f32 v93, v93, s65, v147
; DI unsigned pk4_fp8(float a, float b, float c, float d) { int w = __builtin_amdgcn_cvt_pk_fp8_f32(sat8(a), sat8(b), 0, false); w = __builtin_amdgcn_cvt_pk_fp8_f32(sat8(c), sat8(d), w, true); return (unsigned)w; }
; DI float sig_(float x) { return __builtin_amdgcn_rcpf(1.0f + __builtin_amdgcn_exp2f(-1.4426950408889634f * x)); }
;     DI void operator()(const f32x4 (&acc)[2][2][4][2], const Unit& u, int wr, int wc, int fr, int fq) const {
;     ...
; #pragma unroll
;         for (int ai = 0; ai < 2; ++ai)
; #pragma unroll
;             for (int m = 0; m < 4; ++m) { unsigned char* rowp = base + (size_t)(row0 + ai * HALF + m * 16) * ld;
;                 float o[8];
; #pragma unroll
;                 for (int n = 0; n < 2; ++n)
; #pragma unroll
;                     for (int e = 0; e < 4; ++e) { const float a = acc[ai][0][m][n][e], b = acc[ai][1][m][n][e]; o[n * 4 + e] = a * sig_(a) * (b * H_SC); }
;                 *(u32x2*)rowp = (u32x2){pk4_fp8(o[0], o[1], o[2], o[3]), pk4_fp8(o[4], o[5], o[6], o[7])}; }
	v_cvt_pk_fp8_f32 v88, v92, v93
	v_med3_f32 v94, v94, s65, v147
	v_med3_f32 v95, v95, s65, v147
	v_cvt_pk_fp8_f32 v88, v94, v95 op_sel:[0,0,1]
	v_add_u32_e32 v90, 0x20, v148
	v_mad_i64_i32 v[90:91], s[24:25], v90, s64, v[134:135]
	v_pk_mul_f32 v[112:113], v[84:85], s[98:99] op_sel_hi:[1,0]
	v_pk_mul_f32 v[114:115], v[86:87], s[98:99] op_sel_hi:[1,0]
	v_exp_f32_e32 v112, v112
	v_exp_f32_e32 v113, v113
	v_exp_f32_e32 v114, v114
	v_exp_f32_e32 v115, v115
	v_pk_add_f32 v[112:113], v[112:113], s[100:101] op_sel_hi:[1,0]
	v_pk_add_f32 v[114:115], v[114:115], s[100:101] op_sel_hi:[1,0]
	v_rcp_f32_e32 v112, v112
	v_rcp_f32_e32 v113, v113
	v_rcp_f32_e32 v114, v114
	v_rcp_f32_e32 v115, v115
	v_pk_mul_f32 v[80:81], v[80:81], v[132:133] op_sel:[0,1] op_sel_hi:[1,1]
	v_pk_mul_f32 v[82:83], v[82:83], v[132:133] op_sel:[0,1] op_sel_hi:[1,1]
	v_pk_mul_f32 v[84:85], v[84:85], v[112:113]
	v_pk_mul_f32 v[86:87], v[86:87], v[114:115]
	v_pk_mul_f32 v[84:85], v[84:85], v[80:81]
	v_pk_mul_f32 v[86:87], v[86:87], v[82:83]
	v_med3_f32 v84, v84, s65, v147
	v_med3_f32 v85, v85, s65, v147
	v_cvt_pk_fp8_f32 v89, v84, v85
	v_med3_f32 v86, v86, s65, v147
	v_med3_f32 v87, v87, s65, v147
	v_cvt_pk_fp8_f32 v89, v86, v87 op_sel:[0,0,1]
	global_store_dwordx2 v[90:91], v[88:89], off
	v_pk_mul_f32 v[112:113], v[76:77], s[98:99] op_sel_hi:[1,0]
	v_pk_mul_f32 v[114:115], v[78:79], s[98:99] op_sel_hi:[1,0]
	v_exp_f32_e32 v112, v112
	v_exp_f32_e32 v113, v113
	v_exp_f32_e32 v114, v114
	v_exp_f32_e32 v115, v115
	v_pk_add_f32 v[112:113], v[112:113], s[100:101] op_sel_hi:[1,0]
	v_pk_add_f32 v[114:115], v[114:115], s[100:101] op_sel_hi:[1,0]
	v_rcp_f32_e32 v112, v112
	v_rcp_f32_e32 v113, v113
	v_rcp_f32_e32 v114, v114
	v_rcp_f32_e32 v115, v115
	v_pk_mul_f32 v[72:73], v[72:73], v[132:133] op_sel:[0,1] op_sel_hi:[1,1]
	v_pk_mul_f32 v[74:75], v[74:75], v[132:133] op_sel:[0,1] op_sel_hi:[1,1]
	v_pk_mul_f32 v[76:77], v[76:77], v[112:113]
	v_pk_mul_f32 v[78:79], v[78:79], v[114:115]
	v_pk_mul_f32 v[76:77], v[76:77], v[72:73]
	v_pk_mul_f32 v[78:79], v[78:79], v[74:75]
	v_med3_f32 v76, v76, s65, v147
	v_med3_f32 v77, v77, s65, v147
	v_cvt_pk_fp8_f32 v72, v76, v77
	v_med3_f32 v78, v78, s65, v147
	v_med3_f32 v79, v79, s65, v147
	v_cvt_pk_fp8_f32 v72, v78, v79 op_sel:[0,0,1]
	v_add_u32_e32 v74, 0x30, v148
	v_mad_i64_i32 v[74:75], s[24:25], v74, s64, v[134:135]
	v_pk_mul_f32 v[112:113], v[68:69], s[98:99] op_sel_hi:[1,0]
	v_pk_mul_f32 v[114:115], v[70:71], s[98:99] op_sel_hi:[1,0]
	v_exp_f32_e32 v112, v112
	v_exp_f32_e32 v113, v113
	v_exp_f32_e32 v114, v114
	v_exp_f32_e32 v115, v115
	v_pk_add_f32 v[112:113], v[112:113], s[100:101] op_sel_hi:[1,0]
	v_pk_add_f32 v[114:115], v[114:115], s[100:101] op_sel_hi:[1,0]
	v_rcp_f32_e32 v112, v112
	v_rcp_f32_e32 v113, v113
	v_rcp_f32_e32 v114, v114
	v_rcp_f32_e32 v115, v115
	v_pk_mul_f32 v[64:65], v[64:65], v[132:133] op_sel:[0,1] op_sel_hi:[1,1]
	v_pk_mul_f32 v[66:67], v[66:67], v[132:133] op_sel:[0,1] op_sel_hi:[1,1]
	v_pk_mul_f32 v[68:69], v[68:69], v[112:113]
	v_pk_mul_f32 v[70:71], v[70:71], v[114:115]
	v_pk_mul_f32 v[68:69], v[68:69], v[64:65]
	v_pk_mul_f32 v[70:71], v[70:71], v[66:67]
	v_med3_f32 v68, v68, s65, v147
	v_med3_f32 v69, v69, s65, v147
	v_cvt_pk_fp8_f32 v73, v68, v69
	v_med3_f32 v70, v70, s65, v147
	v_med3_f32 v71, v71, s65, v147
	v_cvt_pk_fp8_f32 v73, v70, v71 op_sel:[0,0,1]
	global_store_dwordx2 v[74:75], v[72:73], off
	v_pk_mul_f32 v[112:113], v[60:61], s[98:99] op_sel_hi:[1,0]
	v_pk_mul_f32 v[114:115], v[62:63], s[98:99] op_sel_hi:[1,0]
	v_exp_f32_e32 v112, v112
	v_exp_f32_e32 v113, v113
	v_exp_f32_e32 v114, v114
	v_exp_f32_e32 v115, v115
	v_pk_add_f32 v[112:113], v[112:113], s[100:101] op_sel_hi:[1,0]
	v_pk_add_f32 v[114:115], v[114:115], s[100:101] op_sel_hi:[1,0]
	v_rcp_f32_e32 v112, v112
	v_rcp_f32_e32 v113, v113
	v_rcp_f32_e32 v114, v114
	v_rcp_f32_e32 v115, v115
	v_pk_mul_f32 v[56:57], v[56:57], v[132:133] op_sel:[0,1] op_sel_hi:[1,1]
	v_pk_mul_f32 v[58:59], v[58:59], v[132:133] op_sel:[0,1] op_sel_hi:[1,1]
	v_pk_mul_f32 v[60:61], v[60:61], v[112:113]
	v_pk_mul_f32 v[62:63], v[62:63], v[114:115]
	v_pk_mul_f32 v[60:61], v[60:61], v[56:57]
	v_pk_mul_f32 v[62:63], v[62:63], v[58:59]
	v_med3_f32 v60, v60, s65, v147
	v_med3_f32 v61, v61, s65, v147
	v_cvt_pk_fp8_f32 v56, v60, v61
	v_med3_f32 v62, v62, s65, v147
	v_med3_f32 v63, v63, s65, v147
	v_cvt_pk_fp8_f32 v56, v62, v63 op_sel:[0,0,1]
	v_add_u32_e32 v58, 0x80, v148
	v_mad_i64_i32 v[58:59], s[24:25], v58, s64, v[134:135]
	v_pk_mul_f32 v[112:113], v[52:53], s[98:99] op_sel_hi:[1,0]
	v_pk_mul_f32 v[114:115], v[54:55], s[98:99] op_sel_hi:[1,0]
	v_exp_f32_e32 v112, v112
	v_exp_f32_e32 v113, v113
	v_exp_f32_e32 v114, v114
	v_exp_f32_e32 v115, v115
	v_pk_add_f32 v[112:113], v[112:113], s[100:101] op_sel_hi:[1,0]
	v_pk_add_f32 v[114:115], v[114:115], s[100:101] op_sel_hi:[1,0]
	v_rcp_f32_e32 v112, v112
	v_rcp_f32_e32 v113, v113
	v_rcp_f32_e32 v114, v114
	v_rcp_f32_e32 v115, v115
	v_pk_mul_f32 v[48:49], v[48:49], v[132:133] op_sel:[0,1] op_sel_hi:[1,1]
	v_pk_mul_f32 v[50:51], v[50:51], v[132:133] op_sel:[0,1] op_sel_hi:[1,1]
	v_pk_mul_f32 v[52:53], v[52:53], v[112:113]
	v_pk_mul_f32 v[54:55], v[54:55], v[114:115]
	v_pk_mul_f32 v[52:53], v[52:53], v[48:49]
	v_pk_mul_f32 v[54:55], v[54:55], v[50:51]
	v_med3_f32 v52, v52, s65, v147
	v_med3_f32 v53, v53, s65, v147
	v_cvt_pk_fp8_f32 v57, v52, v53
	v_med3_f32 v54, v54, s65, v147
	v_med3_f32 v55, v55, s65, v147
	v_cvt_pk_fp8_f32 v57, v54, v55 op_sel:[0,0,1]
	global_store_dwordx2 v[58:59], v[56:57], off
	v_pk_mul_f32 v[112:113], v[44:45], s[98:99] op_sel_hi:[1,0]
	v_pk_mul_f32 v[114:115], v[46:47], s[98:99] op_sel_hi:[1,0]
	v_exp_f32_e32 v112, v112
; DI float sat8(float x) { return __builtin_amdgcn_fmed3f(x, -448.f, 448.f); }
; DI unsigned pk4_fp8(float a, float b, float c, float d) { int w = __builtin_amdgcn_cvt_pk_fp8_f32(sat8(a), sat8(b), 0, false); w = __builtin_amdgcn_cvt_pk_fp8_f32(sat8(c), sat8(d), w, true); return (unsigned)w; }
; DI float sig_(float x) { return __builtin_amdgcn_rcpf(1.0f + __builtin_amdgcn_exp2f(-1.4426950408889634f * x)); }
;     DI void operator()(const f32x4 (&acc)[2][2][4][2], const Unit& u, int wr, int wc, int fr, int fq) const {
;         int row0 = u.pm * BM + wr * 64 + fr; asm volatile("" : "+v"(row0));
;         int coff = wc * 32 + 8 * fq; asm volatile("" : "+v"(coff));
;         unsigned char* base = Hm + u.pn * HALF + coff;
; #pragma unroll
;         for (int ai = 0; ai < 2; ++ai)
; #pragma unroll
;             for (int m = 0; m < 4; ++m) { unsigned char* rowp = base + (size_t)(row0 + ai * HALF + m * 16) * ld;
;                 float o[8];
; #pragma unroll
;                 for (int n = 0; n < 2; ++n)
; #pragma unroll
;                     for (int e = 0; e < 4; ++e) { const float a = acc[ai][0][m][n][e], b = acc[ai][1][m][n][e]; o[n * 4 + e] = a * sig_(a) * (b * H_SC); }
;                 *(u32x2*)rowp = (u32x2){pk4_fp8(o[0], o[1], o[2], o[3]), pk4_fp8(o[4], o[5], o[6], o[7])}; }
;     }
	v_exp_f32_e32 v113, v113
	v_exp_f32_e32 v114, v114
	v_exp_f32_e32 v115, v115
	v_pk_add_f32 v[112:113], v[112:113], s[100:101] op_sel_hi:[1,0]
	v_pk_add_f32 v[114:115], v[114:115], s[100:101] op_sel_hi:[1,0]
	v_rcp_f32_e32 v112, v112
	v_rcp_f32_e32 v113, v113
	v_rcp_f32_e32 v114, v114
	v_rcp_f32_e32 v115, v115
	v_pk_mul_f32 v[40:41], v[40:41], v[132:133] op_sel:[0,1] op_sel_hi:[1,1]
	v_pk_mul_f32 v[42:43], v[42:43], v[132:133] op_sel:[0,1] op_sel_hi:[1,1]
	v_pk_mul_f32 v[44:45], v[44:45], v[112:113]
	v_pk_mul_f32 v[46:47], v[46:47], v[114:115]
	v_pk_mul_f32 v[44:45], v[44:45], v[40:41]
	v_pk_mul_f32 v[46:47], v[46:47], v[42:43]
	v_med3_f32 v44, v44, s65, v147
	v_med3_f32 v45, v45, s65, v147
	v_cvt_pk_fp8_f32 v40, v44, v45
	v_med3_f32 v46, v46, s65, v147
	v_med3_f32 v47, v47, s65, v147
	v_cvt_pk_fp8_f32 v40, v46, v47 op_sel:[0,0,1]
	v_add_u32_e32 v42, 0x90, v148
	v_mad_i64_i32 v[42:43], s[24:25], v42, s64, v[134:135]
	v_pk_mul_f32 v[112:113], v[36:37], s[98:99] op_sel_hi:[1,0]
	v_pk_mul_f32 v[114:115], v[38:39], s[98:99] op_sel_hi:[1,0]
	v_exp_f32_e32 v112, v112
	v_exp_f32_e32 v113, v113
	v_exp_f32_e32 v114, v114
	v_exp_f32_e32 v115, v115
	v_pk_add_f32 v[112:113], v[112:113], s[100:101] op_sel_hi:[1,0]
	v_pk_add_f32 v[114:115], v[114:115], s[100:101] op_sel_hi:[1,0]
	v_rcp_f32_e32 v112, v112
	v_rcp_f32_e32 v113, v113
	v_rcp_f32_e32 v114, v114
	v_rcp_f32_e32 v115, v115
	v_pk_mul_f32 v[32:33], v[32:33], v[132:133] op_sel:[0,1] op_sel_hi:[1,1]
	v_pk_mul_f32 v[34:35], v[34:35], v[132:133] op_sel:[0,1] op_sel_hi:[1,1]
	v_pk_mul_f32 v[36:37], v[36:37], v[112:113]
	v_pk_mul_f32 v[38:39], v[38:39], v[114:115]
	v_pk_mul_f32 v[36:37], v[36:37], v[32:33]
	v_pk_mul_f32 v[38:39], v[38:39], v[34:35]
	v_med3_f32 v36, v36, s65, v147
	v_med3_f32 v37, v37, s65, v147
	v_cvt_pk_fp8_f32 v41, v36, v37
	v_med3_f32 v38, v38, s65, v147
	v_med3_f32 v39, v39, s65, v147
	v_cvt_pk_fp8_f32 v41, v38, v39 op_sel:[0,0,1]
	global_store_dwordx2 v[42:43], v[40:41], off
	v_pk_mul_f32 v[112:113], v[28:29], s[98:99] op_sel_hi:[1,0]
	v_pk_mul_f32 v[114:115], v[30:31], s[98:99] op_sel_hi:[1,0]
	v_exp_f32_e32 v112, v112
	v_exp_f32_e32 v113, v113
	v_exp_f32_e32 v114, v114
	v_exp_f32_e32 v115, v115
	v_pk_add_f32 v[112:113], v[112:113], s[100:101] op_sel_hi:[1,0]
	v_pk_add_f32 v[114:115], v[114:115], s[100:101] op_sel_hi:[1,0]
	v_rcp_f32_e32 v112, v112
	v_rcp_f32_e32 v113, v113
	v_rcp_f32_e32 v114, v114
	v_rcp_f32_e32 v115, v115
	v_pk_mul_f32 v[24:25], v[24:25], v[132:133] op_sel:[0,1] op_sel_hi:[1,1]
	v_pk_mul_f32 v[26:27], v[26:27], v[132:133] op_sel:[0,1] op_sel_hi:[1,1]
	v_pk_mul_f32 v[28:29], v[28:29], v[112:113]
	v_pk_mul_f32 v[30:31], v[30:31], v[114:115]
	v_pk_mul_f32 v[28:29], v[28:29], v[24:25]
	v_pk_mul_f32 v[30:31], v[30:31], v[26:27]
	v_med3_f32 v28, v28, s65, v147
	v_med3_f32 v29, v29, s65, v147
	v_cvt_pk_fp8_f32 v24, v28, v29
	v_med3_f32 v30, v30, s65, v147
	v_med3_f32 v31, v31, s65, v147
	v_cvt_pk_fp8_f32 v24, v30, v31 op_sel:[0,0,1]
	v_add_u32_e32 v26, 0xa0, v148
	v_mad_i64_i32 v[26:27], s[24:25], v26, s64, v[134:135]
	v_pk_mul_f32 v[112:113], v[20:21], s[98:99] op_sel_hi:[1,0]
	v_pk_mul_f32 v[114:115], v[22:23], s[98:99] op_sel_hi:[1,0]
	v_exp_f32_e32 v112, v112
	v_exp_f32_e32 v113, v113
	v_exp_f32_e32 v114, v114
	v_exp_f32_e32 v115, v115
	v_pk_add_f32 v[112:113], v[112:113], s[100:101] op_sel_hi:[1,0]
	v_pk_add_f32 v[114:115], v[114:115], s[100:101] op_sel_hi:[1,0]
	v_rcp_f32_e32 v112, v112
	v_rcp_f32_e32 v113, v113
	v_rcp_f32_e32 v114, v114
	v_rcp_f32_e32 v115, v115
	v_pk_mul_f32 v[16:17], v[16:17], v[132:133] op_sel:[0,1] op_sel_hi:[1,1]
	v_pk_mul_f32 v[18:19], v[18:19], v[132:133] op_sel:[0,1] op_sel_hi:[1,1]
	v_pk_mul_f32 v[20:21], v[20:21], v[112:113]
	v_pk_mul_f32 v[22:23], v[22:23], v[114:115]
	v_pk_mul_f32 v[20:21], v[20:21], v[16:17]
	v_pk_mul_f32 v[22:23], v[22:23], v[18:19]
	v_med3_f32 v20, v20, s65, v147
	v_med3_f32 v21, v21, s65, v147
	v_cvt_pk_fp8_f32 v25, v20, v21
	v_med3_f32 v22, v22, s65, v147
	v_med3_f32 v23, v23, s65, v147
	v_cvt_pk_fp8_f32 v25, v22, v23 op_sel:[0,0,1]
	global_store_dwordx2 v[26:27], v[24:25], off
	v_pk_mul_f32 v[112:113], v[12:13], s[98:99] op_sel_hi:[1,0]
	v_pk_mul_f32 v[114:115], v[14:15], s[98:99] op_sel_hi:[1,0]
	v_exp_f32_e32 v112, v112
	v_exp_f32_e32 v113, v113
	v_exp_f32_e32 v114, v114
	v_exp_f32_e32 v115, v115
	v_pk_add_f32 v[112:113], v[112:113], s[100:101] op_sel_hi:[1,0]
	v_pk_add_f32 v[114:115], v[114:115], s[100:101] op_sel_hi:[1,0]
	v_rcp_f32_e32 v112, v112
	v_rcp_f32_e32 v113, v113
	v_rcp_f32_e32 v114, v114
	v_rcp_f32_e32 v115, v115
	v_pk_mul_f32 v[8:9], v[8:9], v[132:133] op_sel:[0,1] op_sel_hi:[1,1]
	v_pk_mul_f32 v[10:11], v[10:11], v[132:133] op_sel:[0,1] op_sel_hi:[1,1]
	v_pk_mul_f32 v[12:13], v[12:13], v[112:113]
	v_pk_mul_f32 v[14:15], v[14:15], v[114:115]
	v_pk_mul_f32 v[12:13], v[12:13], v[8:9]
	v_pk_mul_f32 v[14:15], v[14:15], v[10:11]
	v_med3_f32 v12, v12, s65, v147
	v_med3_f32 v13, v13, s65, v147
	v_cvt_pk_fp8_f32 v8, v12, v13
	v_med3_f32 v14, v14, s65, v147
	v_med3_f32 v15, v15, s65, v147
	v_cvt_pk_fp8_f32 v8, v14, v15 op_sel:[0,0,1]
	v_add_u32_e32 v10, 0xb0, v148
	v_mad_i64_i32 v[10:11], s[24:25], v10, s64, v[134:135]
	v_pk_mul_f32 v[112:113], v[4:5], s[98:99] op_sel_hi:[1,0]
	v_pk_mul_f32 v[114:115], v[6:7], s[98:99] op_sel_hi:[1,0]
	v_exp_f32_e32 v112, v112
	v_exp_f32_e32 v113, v113
	v_exp_f32_e32 v114, v114
	v_exp_f32_e32 v115, v115
	v_pk_add_f32 v[112:113], v[112:113], s[100:101] op_sel_hi:[1,0]
	v_pk_add_f32 v[114:115], v[114:115], s[100:101] op_sel_hi:[1,0]
	v_rcp_f32_e32 v112, v112
	v_rcp_f32_e32 v113, v113
	v_rcp_f32_e32 v114, v114
	v_rcp_f32_e32 v115, v115
	v_pk_mul_f32 v[0:1], v[0:1], v[132:133] op_sel:[0,1] op_sel_hi:[1,1]
	v_pk_mul_f32 v[2:3], v[2:3], v[132:133] op_sel:[0,1] op_sel_hi:[1,1]
	v_pk_mul_f32 v[4:5], v[4:5], v[112:113]
	v_pk_mul_f32 v[6:7], v[6:7], v[114:115]
	v_pk_mul_f32 v[4:5], v[4:5], v[0:1]
	v_pk_mul_f32 v[6:7], v[6:7], v[2:3]
	v_med3_f32 v4, v4, s65, v147
	v_med3_f32 v5, v5, s65, v147
	v_cvt_pk_fp8_f32 v9, v4, v5
	v_med3_f32 v6, v6, s65, v147
	v_med3_f32 v7, v7, s65, v147
	v_cvt_pk_fp8_f32 v9, v6, v7 op_sel:[0,0,1]
	global_store_dwordx2 v[10:11], v[8:9], off
	s_cbranch_vccnz .LBB0_696
	s_andn2_b64 vcc, exec, s[8:9]
	s_cbranch_vccnz .LBB0_695
	s_barrier
	s_branch .LBB0_695

; DI float sat8(float x) { return __builtin_amdgcn_fmed3f(x, -448.f, 448.f); }
; DI unsigned pk4_fp8(float a, float b, float c, float d) { int w = __builtin_amdgcn_cvt_pk_fp8_f32(sat8(a), sat8(b), 0, false); w = __builtin_amdgcn_cvt_pk_fp8_f32(sat8(c), sat8(d), w, true); return (unsigned)w; }
; DI float sig_(float x) { return __builtin_amdgcn_rcpf(1.0f + __builtin_amdgcn_exp2f(-1.4426950408889634f * x)); }
;     DI void operator()(const f32x4 (&acc)[2][2][4][2], const Unit& u, int wr, int wc, int fr, int fq) const {
;         int row0 = u.pm * BM + wr * 64 + fr; asm volatile("" : "+v"(row0));
;         int coff = wc * 32 + 8 * fq; asm volatile("" : "+v"(coff));
;         unsigned char* base = Hm + u.pn * HALF + coff;
; #pragma unroll
;         for (int ai = 0; ai < 2; ++ai)
; #pragma unroll
;             for (int m = 0; m < 4; ++m) { unsigned char* rowp = base + (size_t)(row0 + ai * HALF + m * 16) * ld;
;                 float o[8];
; #pragma unroll
;                 for (int n = 0; n < 2; ++n)
; #pragma unroll
;                     for (int e = 0; e < 4; ++e) { const float a = acc[ai][0][m][n][e], b = acc[ai][1][m][n][e]; o[n * 4 + e] = a * sig_(a) * b; }
;                 *(u32x2*)rowp = (u32x2){pk4_fp8(o[0], o[1], o[2], o[3]), pk4_fp8(o[4], o[5], o[6], o[7])}; }
;     }
.LBB0_1611:
	s_lshl_b32 s6, s22, 7
	s_ashr_i32 s7, s6, 31
	v_lshl_add_u32 v143, s24, 8, v138
	v_mov_b32_e32 v128, v139
	s_add_u32 s6, s53, s6
	s_addc_u32 s7, s54, s7
	v_ashrrev_i32_e32 v129, 31, v128
	s_mov_b32 s98, 0xbfb8aa3b
	s_mov_b32 s100, 1.0
	v_lshl_add_u64 v[130:131], s[6:7], 0, v[128:129]
	v_pk_mul_f32 v[144:145], v[124:125], s[98:99] op_sel_hi:[1,0]
	v_pk_mul_f32 v[128:129], v[126:127], s[98:99] op_sel_hi:[1,0]
	v_exp_f32_e32 v144, v144
	v_exp_f32_e32 v145, v145
	v_exp_f32_e32 v128, v128
	v_exp_f32_e32 v129, v129
	v_pk_add_f32 v[144:145], v[144:145], s[100:101] op_sel_hi:[1,0]
	v_pk_add_f32 v[128:129], v[128:129], s[100:101] op_sel_hi:[1,0]
	v_rcp_f32_e32 v144, v144
	v_rcp_f32_e32 v145, v145
	v_rcp_f32_e32 v128, v128
	v_rcp_f32_e32 v129, v129
	v_pk_mul_f32 v[124:125], v[124:125], v[144:145]
	v_pk_mul_f32 v[126:127], v[126:127], v[128:129]
	v_pk_mul_f32 v[124:125], v[124:125], v[116:117]
	v_pk_mul_f32 v[126:127], v[126:127], v[118:119]
	v_med3_f32 v124, v124, s66, v142
	v_med3_f32 v125, v125, s66, v142
	v_cvt_pk_fp8_f32 v116, v124, v125
	v_med3_f32 v126, v126, s66, v142
	v_med3_f32 v127, v127, s66, v142
	v_cvt_pk_fp8_f32 v116, v126, v127 op_sel:[0,0,1]
	v_mad_i64_i32 v[118:119], s[6:7], v143, s65, v[130:131]
	v_pk_mul_f32 v[144:145], v[120:121], s[98:99] op_sel_hi:[1,0]
	v_pk_mul_f32 v[128:129], v[122:123], s[98:99] op_sel_hi:[1,0]
	v_exp_f32_e32 v144, v144
	v_exp_f32_e32 v145, v145
	v_exp_f32_e32 v128, v128
	v_exp_f32_e32 v129, v129
	v_pk_add_f32 v[144:145], v[144:145], s[100:101] op_sel_hi:[1,0]
	v_pk_add_f32 v[128:129], v[128:129], s[100:101] op_sel_hi:[1,0]
	v_rcp_f32_e32 v144, v144
	v_rcp_f32_e32 v145, v145
	v_rcp_f32_e32 v128, v128
	v_rcp_f32_e32 v129, v129
	v_pk_mul_f32 v[120:121], v[120:121], v[144:145]
	v_pk_mul_f32 v[122:123], v[122:123], v[128:129]
	v_pk_mul_f32 v[120:121], v[120:121], v[112:113]
	v_pk_mul_f32 v[122:123], v[122:123], v[114:115]
	v_med3_f32 v120, v120, s66, v142
	v_med3_f32 v121, v121, s66, v142
	v_cvt_pk_fp8_f32 v117, v120, v121
	v_med3_f32 v122, v122, s66, v142
	v_med3_f32 v123, v123, s66, v142
	v_cvt_pk_fp8_f32 v117, v122, v123 op_sel:[0,0,1]
	global_store_dwordx2 v[118:119], v[116:117], off
	v_pk_mul_f32 v[144:145], v[108:109], s[98:99] op_sel_hi:[1,0]
	v_pk_mul_f32 v[128:129], v[110:111], s[98:99] op_sel_hi:[1,0]
	v_exp_f32_e32 v144, v144
	v_exp_f32_e32 v145, v145
	v_exp_f32_e32 v128, v128
	v_exp_f32_e32 v129, v129
	v_pk_add_f32 v[144:145], v[144:145], s[100:101] op_sel_hi:[1,0]
	v_pk_add_f32 v[128:129], v[128:129], s[100:101] op_sel_hi:[1,0]
	v_rcp_f32_e32 v144, v144
	v_rcp_f32_e32 v145, v145
	v_rcp_f32_e32 v128, v128
	v_rcp_f32_e32 v129, v129
	v_pk_mul_f32 v[108:109], v[108:109], v[144:145]
	v_pk_mul_f32 v[110:111], v[110:111], v[128:129]
	v_pk_mul_f32 v[108:109], v[108:109], v[100:101]
	v_pk_mul_f32 v[110:111], v[110:111], v[102:103]
	v_med3_f32 v108, v108, s66, v142
	v_med3_f32 v109, v109, s66, v142
	v_cvt_pk_fp8_f32 v100, v108, v109
	v_med3_f32 v110, v110, s66, v142
	v_med3_f32 v111, v111, s66, v142
	v_cvt_pk_fp8_f32 v100, v110, v111 op_sel:[0,0,1]
	v_add_u32_e32 v102, 0x10, v143
	v_mad_i64_i32 v[102:103], s[6:7], v102, s65, v[130:131]
	v_pk_mul_f32 v[144:145], v[104:105], s[98:99] op_sel_hi:[1,0]
	v_pk_mul_f32 v[128:129], v[106:107], s[98:99] op_sel_hi:[1,0]
	v_exp_f32_e32 v144, v144
	v_exp_f32_e32 v145, v145
	v_exp_f32_e32 v128, v128
	v_exp_f32_e32 v129, v129
	v_pk_add_f32 v[144:145], v[144:145], s[100:101] op_sel_hi:[1,0]
	v_pk_add_f32 v[128:129], v[128:129], s[100:101] op_sel_hi:[1,0]
	v_rcp_f32_e32 v144, v144
	v_rcp_f32_e32 v145, v145
	v_rcp_f32_e32 v128, v128
	v_rcp_f32_e32 v129, v129
	v_pk_mul_f32 v[104:105], v[104:105], v[144:145]
	v_pk_mul_f32 v[106:107], v[106:107], v[128:129]
	v_pk_mul_f32 v[104:105], v[104:105], v[96:97]
	v_pk_mul_f32 v[106:107], v[106:107], v[98:99]
	v_med3_f32 v104, v104, s66, v142
	v_med3_f32 v105, v105, s66, v142
	v_cvt_pk_fp8_f32 v101, v104, v105
	v_med3_f32 v106, v106, s66, v142
	v_med3_f32 v107, v107, s66, v142
	v_cvt_pk_fp8_f32 v101, v106, v107 op_sel:[0,0,1]
	global_store_dwordx2 v[102:103], v[100:101], off
	v_pk_mul_f32 v[144:145], v[92:93], s[98:99] op_sel_hi:[1,0]
	v_pk_mul_f32 v[128:129], v[94:95], s[98:99] op_sel_hi:[1,0]
	v_exp_f32_e32 v144, v144
	v_exp_f32_e32 v145, v145
	v_exp_f32_e32 v128, v128
	v_exp_f32_e32 v129, v129
	v_pk_add_f32 v[144:145], v[144:145], s[100:101] op_sel_hi:[1,0]
	v_pk_add_f32 v[128:129], v[128:129], s[100:101] op_sel_hi:[1,0]
	v_rcp_f32_e32 v144, v144
	v_rcp_f32_e32 v145, v145
	v_rcp_f32_e32 v128, v128
	v_rcp_f32_e32 v129, v129
	v_pk_mul_f32 v[92:93], v[92:93], v[144:145]
	v_pk_mul_f32 v[94:95], v[94:95], v[128:129]
	v_pk_mul_f32 v[92:93], v[92:93], v[84:85]
	v_pk_mul_f32 v[94:95], v[94:95], v[86:87]
	v_med3_f32 v92, v92, s66, v142
	v_med3_f32 v93, v93, s66, v142
	v_cvt_pk_fp8_f32 v84, v92, v93
	v_med3_f32 v94, v94, s66, v142
	v_med3_f32 v95, v95, s66, v142
	v_cvt_pk_fp8_f32 v84, v94, v95 op_sel:[0,0,1]
	v_add_u32_e32 v86, 0x20, v143
	v_mad_i64_i32 v[86:87], s[6:7], v86, s65, v[130:131]
	v_pk_mul_f32 v[144:145], v[88:89], s[98:99] op_sel_hi:[1,0]
	v_pk_mul_f32 v[128:129], v[90:91], s[98:99] op_sel_hi:[1,0]
	v_exp_f32_e32 v144, v144
	v_exp_f32_e32 v145, v145
	v_exp_f32_e32 v128, v128
	v_exp_f32_e32 v129, v129
	v_pk_add_f32 v[144:145], v[144:145], s[100:101] op_sel_hi:[1,0]
	v_pk_add_f32 v[128:129], v[128:129], s[100:101] op_sel_hi:[1,0]
	v_rcp_f32_e32 v144, v144
	v_rcp_f32_e32 v145, v145
	v_rcp_f32_e32 v128, v128
	v_rcp_f32_e32 v129, v129
	v_pk_mul_f32 v[88:89], v[88:89], v[144:145]
	v_pk_mul_f32 v[90:91], v[90:91], v[128:129]
	v_pk_mul_f32 v[88:89], v[88:89], v[80:81]
	v_pk_mul_f32 v[90:91], v[90:91], v[82:83]
; DI float sat8(float x) { return __builtin_amdgcn_fmed3f(x, -448.f, 448.f); }
; DI unsigned pk4_fp8(float a, float b, float c, float d) { int w = __builtin_amdgcn_cvt_pk_fp8_f32(sat8(a), sat8(b), 0, false); w = __builtin_amdgcn_cvt_pk_fp8_f32(sat8(c), sat8(d), w, true); return (unsigned)w; }
; DI float sig_(float x) { return __builtin_amdgcn_rcpf(1.0f + __builtin_amdgcn_exp2f(-1.4426950408889634f * x)); }
;     DI void operator()(const f32x4 (&acc)[2][2][4][2], const Unit& u, int wr, int wc, int fr, int fq) const {
;         int row0 = u.pm * BM + wr * 64 + fr; asm volatile("" : "+v"(row0));
;         int coff = wc * 32 + 8 * fq; asm volatile("" : "+v"(coff));
;         unsigned char* base = Hm + u.pn * HALF + coff;
; #pragma unroll
;         for (int ai = 0; ai < 2; ++ai)
; #pragma unroll
;             for (int m = 0; m < 4; ++m) { unsigned char* rowp = base + (size_t)(row0 + ai * HALF + m * 16) * ld;
;                 float o[8];
; #pragma unroll
;                 for (int n = 0; n < 2; ++n)
; #pragma unroll
;                     for (int e = 0; e < 4; ++e) { const float a = acc[ai][0][m][n][e], b = acc[ai][1][m][n][e]; o[n * 4 + e] = a * sig_(a) * b; }
;                 *(u32x2*)rowp = (u32x2){pk4_fp8(o[0], o[1], o[2], o[3]), pk4_fp8(o[4], o[5], o[6], o[7])}; }
;     }
	v_med3_f32 v88, v88, s66, v142
	v_med3_f32 v89, v89, s66, v142
	v_cvt_pk_fp8_f32 v85, v88, v89
	v_med3_f32 v90, v90, s66, v142
	v_med3_f32 v91, v91, s66, v142
	v_cvt_pk_fp8_f32 v85, v90, v91 op_sel:[0,0,1]
	global_store_dwordx2 v[86:87], v[84:85], off
	v_pk_mul_f32 v[144:145], v[76:77], s[98:99] op_sel_hi:[1,0]
	v_pk_mul_f32 v[128:129], v[78:79], s[98:99] op_sel_hi:[1,0]
	v_exp_f32_e32 v144, v144
	v_exp_f32_e32 v145, v145
	v_exp_f32_e32 v128, v128
	v_exp_f32_e32 v129, v129
	v_pk_add_f32 v[144:145], v[144:145], s[100:101] op_sel_hi:[1,0]
	v_pk_add_f32 v[128:129], v[128:129], s[100:101] op_sel_hi:[1,0]
	v_rcp_f32_e32 v144, v144
	v_rcp_f32_e32 v145, v145
	v_rcp_f32_e32 v128, v128
	v_rcp_f32_e32 v129, v129
	v_pk_mul_f32 v[76:77], v[76:77], v[144:145]
	v_pk_mul_f32 v[78:79], v[78:79], v[128:129]
	v_pk_mul_f32 v[76:77], v[76:77], v[68:69]
	v_pk_mul_f32 v[78:79], v[78:79], v[70:71]
	v_med3_f32 v76, v76, s66, v142
	v_med3_f32 v77, v77, s66, v142
	v_cvt_pk_fp8_f32 v68, v76, v77
	v_med3_f32 v78, v78, s66, v142
	v_med3_f32 v79, v79, s66, v142
	v_cvt_pk_fp8_f32 v68, v78, v79 op_sel:[0,0,1]
	v_add_u32_e32 v70, 0x30, v143
	v_mad_i64_i32 v[70:71], s[6:7], v70, s65, v[130:131]
	v_pk_mul_f32 v[144:145], v[72:73], s[98:99] op_sel_hi:[1,0]
	v_pk_mul_f32 v[128:129], v[74:75], s[98:99] op_sel_hi:[1,0]
	v_exp_f32_e32 v144, v144
	v_exp_f32_e32 v145, v145
	v_exp_f32_e32 v128, v128
	v_exp_f32_e32 v129, v129
	v_pk_add_f32 v[144:145], v[144:145], s[100:101] op_sel_hi:[1,0]
	v_pk_add_f32 v[128:129], v[128:129], s[100:101] op_sel_hi:[1,0]
	v_rcp_f32_e32 v144, v144
	v_rcp_f32_e32 v145, v145
	v_rcp_f32_e32 v128, v128
	v_rcp_f32_e32 v129, v129
	v_pk_mul_f32 v[72:73], v[72:73], v[144:145]
	v_pk_mul_f32 v[74:75], v[74:75], v[128:129]
	v_pk_mul_f32 v[72:73], v[72:73], v[64:65]
	v_pk_mul_f32 v[74:75], v[74:75], v[66:67]
	v_med3_f32 v72, v72, s66, v142
	v_med3_f32 v73, v73, s66, v142
	v_cvt_pk_fp8_f32 v69, v72, v73
	v_med3_f32 v74, v74, s66, v142
	v_med3_f32 v75, v75, s66, v142
	v_cvt_pk_fp8_f32 v69, v74, v75 op_sel:[0,0,1]
	global_store_dwordx2 v[70:71], v[68:69], off
	v_pk_mul_f32 v[144:145], v[60:61], s[98:99] op_sel_hi:[1,0]
	v_pk_mul_f32 v[128:129], v[62:63], s[98:99] op_sel_hi:[1,0]
	v_exp_f32_e32 v144, v144
	v_exp_f32_e32 v145, v145
	v_exp_f32_e32 v128, v128
	v_exp_f32_e32 v129, v129
	v_pk_add_f32 v[144:145], v[144:145], s[100:101] op_sel_hi:[1,0]
	v_pk_add_f32 v[128:129], v[128:129], s[100:101] op_sel_hi:[1,0]
	v_rcp_f32_e32 v144, v144
	v_rcp_f32_e32 v145, v145
	v_rcp_f32_e32 v128, v128
	v_rcp_f32_e32 v129, v129
	v_pk_mul_f32 v[60:61], v[60:61], v[144:145]
	v_pk_mul_f32 v[62:63], v[62:63], v[128:129]
	v_pk_mul_f32 v[60:61], v[60:61], v[52:53]
	v_pk_mul_f32 v[62:63], v[62:63], v[54:55]
	v_med3_f32 v60, v60, s66, v142
	v_med3_f32 v61, v61, s66, v142
	v_cvt_pk_fp8_f32 v52, v60, v61
	v_med3_f32 v62, v62, s66, v142
	v_med3_f32 v63, v63, s66, v142
	v_cvt_pk_fp8_f32 v52, v62, v63 op_sel:[0,0,1]
	v_add_u32_e32 v54, 0x80, v143
	v_mad_i64_i32 v[54:55], s[6:7], v54, s65, v[130:131]
	v_pk_mul_f32 v[144:145], v[56:57], s[98:99] op_sel_hi:[1,0]
	v_pk_mul_f32 v[128:129], v[58:59], s[98:99] op_sel_hi:[1,0]
	v_exp_f32_e32 v144, v144
	v_exp_f32_e32 v145, v145
	v_exp_f32_e32 v128, v128
	v_exp_f32_e32 v129, v129
	v_pk_add_f32 v[144:145], v[144:145], s[100:101] op_sel_hi:[1,0]
	v_pk_add_f32 v[128:129], v[128:129], s[100:101] op_sel_hi:[1,0]
	v_rcp_f32_e32 v144, v144
	v_rcp_f32_e32 v145, v145
	v_rcp_f32_e32 v128, v128
	v_rcp_f32_e32 v129, v129
	v_pk_mul_f32 v[56:57], v[56:57], v[144:145]
	v_pk_mul_f32 v[58:59], v[58:59], v[128:129]
	v_pk_mul_f32 v[56:57], v[56:57], v[48:49]
	v_pk_mul_f32 v[58:59], v[58:59], v[50:51]
	v_med3_f32 v56, v56, s66, v142
	v_med3_f32 v57, v57, s66, v142
	v_cvt_pk_fp8_f32 v53, v56, v57
	v_med3_f32 v58, v58, s66, v142
	v_med3_f32 v59, v59, s66, v142
	v_cvt_pk_fp8_f32 v53, v58, v59 op_sel:[0,0,1]
	global_store_dwordx2 v[54:55], v[52:53], off
	v_pk_mul_f32 v[144:145], v[44:45], s[98:99] op_sel_hi:[1,0]
	v_pk_mul_f32 v[128:129], v[46:47], s[98:99] op_sel_hi:[1,0]
	v_exp_f32_e32 v144, v144
	v_exp_f32_e32 v145, v145
	v_exp_f32_e32 v128, v128
	v_exp_f32_e32 v129, v129
	v_pk_add_f32 v[144:145], v[144:145], s[100:101] op_sel_hi:[1,0]
	v_pk_add_f32 v[128:129], v[128:129], s[100:101] op_sel_hi:[1,0]
	v_rcp_f32_e32 v144, v144
	v_rcp_f32_e32 v145, v145
	v_rcp_f32_e32 v128, v128
	v_rcp_f32_e32 v129, v129
	v_pk_mul_f32 v[44:45], v[44:45], v[144:145]
	v_pk_mul_f32 v[46:47], v[46:47], v[128:129]
	v_pk_mul_f32 v[44:45], v[44:45], v[36:37]
	v_pk_mul_f32 v[46:47], v[46:47], v[38:39]
	v_med3_f32 v44, v44, s66, v142
	v_med3_f32 v45, v45, s66, v142
	v_cvt_pk_fp8_f32 v36, v44, v45
	v_med3_f32 v46, v46, s66, v142
	v_med3_f32 v47, v47, s66, v142
	v_cvt_pk_fp8_f32 v36, v46, v47 op_sel:[0,0,1]
; DI float sat8(float x) { return __builtin_amdgcn_fmed3f(x, -448.f, 448.f); }
; DI unsigned pk4_fp8(float a, float b, float c, float d) { int w = __builtin_amdgcn_cvt_pk_fp8_f32(sat8(a), sat8(b), 0, false); w = __builtin_amdgcn_cvt_pk_fp8_f32(sat8(c), sat8(d), w, true); return (unsigned)w; }
; DI float sig_(float x) { return __builtin_amdgcn_rcpf(1.0f + __builtin_amdgcn_exp2f(-1.4426950408889634f * x)); }
;     DI void operator()(const f32x4 (&acc)[2][2][4][2], const Unit& u, int wr, int wc, int fr, int fq) const {
;         int row0 = u.pm * BM + wr * 64 + fr; asm volatile("" : "+v"(row0));
;         int coff = wc * 32 + 8 * fq; asm volatile("" : "+v"(coff));
;         unsigned char* base = Hm + u.pn * HALF + coff;
; #pragma unroll
;         for (int ai = 0; ai < 2; ++ai)
; #pragma unroll
;             for (int m = 0; m < 4; ++m) { unsigned char* rowp = base + (size_t)(row0 + ai * HALF + m * 16) * ld;
;                 float o[8];
; #pragma unroll
;                 for (int n = 0; n < 2; ++n)
; #pragma unroll
;                     for (int e = 0; e < 4; ++e) { const float a = acc[ai][0][m][n][e], b = acc[ai][1][m][n][e]; o[n * 4 + e] = a * sig_(a) * b; }
;                 *(u32x2*)rowp = (u32x2){pk4_fp8(o[0], o[1], o[2], o[3]), pk4_fp8(o[4], o[5], o[6], o[7])}; }
;     }
	v_add_u32_e32 v38, 0x90, v143
	v_mad_i64_i32 v[38:39], s[6:7], v38, s65, v[130:131]
	v_pk_mul_f32 v[144:145], v[40:41], s[98:99] op_sel_hi:[1,0]
	v_pk_mul_f32 v[128:129], v[42:43], s[98:99] op_sel_hi:[1,0]
	v_exp_f32_e32 v144, v144
	v_exp_f32_e32 v145, v145
	v_exp_f32_e32 v128, v128
	v_exp_f32_e32 v129, v129
	v_pk_add_f32 v[144:145], v[144:145], s[100:101] op_sel_hi:[1,0]
	v_pk_add_f32 v[128:129], v[128:129], s[100:101] op_sel_hi:[1,0]
	v_rcp_f32_e32 v144, v144
	v_rcp_f32_e32 v145, v145
	v_rcp_f32_e32 v128, v128
	v_rcp_f32_e32 v129, v129
	v_pk_mul_f32 v[40:41], v[40:41], v[144:145]
	v_pk_mul_f32 v[42:43], v[42:43], v[128:129]
	v_pk_mul_f32 v[40:41], v[40:41], v[32:33]
	v_pk_mul_f32 v[42:43], v[42:43], v[34:35]
	v_med3_f32 v40, v40, s66, v142
	v_med3_f32 v41, v41, s66, v142
	v_cvt_pk_fp8_f32 v37, v40, v41
	v_med3_f32 v42, v42, s66, v142
	v_med3_f32 v43, v43, s66, v142
	v_cvt_pk_fp8_f32 v37, v42, v43 op_sel:[0,0,1]
	global_store_dwordx2 v[38:39], v[36:37], off
	v_pk_mul_f32 v[144:145], v[28:29], s[98:99] op_sel_hi:[1,0]
	v_pk_mul_f32 v[128:129], v[30:31], s[98:99] op_sel_hi:[1,0]
	v_exp_f32_e32 v144, v144
	v_exp_f32_e32 v145, v145
	v_exp_f32_e32 v128, v128
	v_exp_f32_e32 v129, v129
	v_pk_add_f32 v[144:145], v[144:145], s[100:101] op_sel_hi:[1,0]
	v_pk_add_f32 v[128:129], v[128:129], s[100:101] op_sel_hi:[1,0]
	v_rcp_f32_e32 v144, v144
	v_rcp_f32_e32 v145, v145
	v_rcp_f32_e32 v128, v128
	v_rcp_f32_e32 v129, v129
	v_pk_mul_f32 v[28:29], v[28:29], v[144:145]
	v_pk_mul_f32 v[30:31], v[30:31], v[128:129]
	v_pk_mul_f32 v[28:29], v[28:29], v[20:21]
	v_pk_mul_f32 v[30:31], v[30:31], v[22:23]
	v_med3_f32 v28, v28, s66, v142
	v_med3_f32 v29, v29, s66, v142
	v_cvt_pk_fp8_f32 v20, v28, v29
	v_med3_f32 v30, v30, s66, v142
	v_med3_f32 v31, v31, s66, v142
	v_cvt_pk_fp8_f32 v20, v30, v31 op_sel:[0,0,1]
	v_add_u32_e32 v22, 0xa0, v143
	v_mad_i64_i32 v[22:23], s[6:7], v22, s65, v[130:131]
	v_pk_mul_f32 v[144:145], v[24:25], s[98:99] op_sel_hi:[1,0]
	v_pk_mul_f32 v[128:129], v[26:27], s[98:99] op_sel_hi:[1,0]
	v_exp_f32_e32 v144, v144
	v_exp_f32_e32 v145, v145
	v_exp_f32_e32 v128, v128
	v_exp_f32_e32 v129, v129
	v_pk_add_f32 v[144:145], v[144:145], s[100:101] op_sel_hi:[1,0]
	v_pk_add_f32 v[128:129], v[128:129], s[100:101] op_sel_hi:[1,0]
	v_rcp_f32_e32 v144, v144
	v_rcp_f32_e32 v145, v145
	v_rcp_f32_e32 v128, v128
	v_rcp_f32_e32 v129, v129
	v_pk_mul_f32 v[24:25], v[24:25], v[144:145]
	v_pk_mul_f32 v[26:27], v[26:27], v[128:129]
	v_pk_mul_f32 v[24:25], v[24:25], v[16:17]
	v_pk_mul_f32 v[26:27], v[26:27], v[18:19]
	v_med3_f32 v24, v24, s66, v142
	v_med3_f32 v25, v25, s66, v142
	v_cvt_pk_fp8_f32 v21, v24, v25
	v_med3_f32 v26, v26, s66, v142
	v_med3_f32 v27, v27, s66, v142
	v_cvt_pk_fp8_f32 v21, v26, v27 op_sel:[0,0,1]
	global_store_dwordx2 v[22:23], v[20:21], off
	v_pk_mul_f32 v[144:145], v[12:13], s[98:99] op_sel_hi:[1,0]
	v_pk_mul_f32 v[128:129], v[14:15], s[98:99] op_sel_hi:[1,0]
	v_exp_f32_e32 v144, v144
	v_exp_f32_e32 v145, v145
	v_exp_f32_e32 v128, v128
	v_exp_f32_e32 v129, v129
	v_pk_add_f32 v[144:145], v[144:145], s[100:101] op_sel_hi:[1,0]
	v_pk_add_f32 v[128:129], v[128:129], s[100:101] op_sel_hi:[1,0]
	v_rcp_f32_e32 v144, v144
	v_rcp_f32_e32 v145, v145
	v_rcp_f32_e32 v128, v128
	v_rcp_f32_e32 v129, v129
	v_pk_mul_f32 v[12:13], v[12:13], v[144:145]
	v_pk_mul_f32 v[14:15], v[14:15], v[128:129]
	v_pk_mul_f32 v[12:13], v[12:13], v[4:5]
	v_pk_mul_f32 v[14:15], v[14:15], v[6:7]
	v_med3_f32 v12, v12, s66, v142
	v_med3_f32 v13, v13, s66, v142
	v_cvt_pk_fp8_f32 v4, v12, v13
	v_med3_f32 v14, v14, s66, v142
	v_med3_f32 v15, v15, s66, v142
	v_cvt_pk_fp8_f32 v4, v14, v15 op_sel:[0,0,1]
	v_add_u32_e32 v6, 0xb0, v143
	v_mad_i64_i32 v[6:7], s[6:7], v6, s65, v[130:131]
	v_pk_mul_f32 v[144:145], v[8:9], s[98:99] op_sel_hi:[1,0]
	v_pk_mul_f32 v[128:129], v[10:11], s[98:99] op_sel_hi:[1,0]
	v_exp_f32_e32 v144, v144
	v_exp_f32_e32 v145, v145
	v_exp_f32_e32 v128, v128
	v_exp_f32_e32 v129, v129
	v_pk_add_f32 v[144:145], v[144:145], s[100:101] op_sel_hi:[1,0]
	v_pk_add_f32 v[128:129], v[128:129], s[100:101] op_sel_hi:[1,0]
	v_rcp_f32_e32 v144, v144
	v_rcp_f32_e32 v145, v145
	v_rcp_f32_e32 v128, v128
	v_rcp_f32_e32 v129, v129
	v_pk_mul_f32 v[8:9], v[8:9], v[144:145]
	v_pk_mul_f32 v[10:11], v[10:11], v[128:129]
	v_pk_mul_f32 v[8:9], v[8:9], v[0:1]
	v_pk_mul_f32 v[10:11], v[10:11], v[2:3]
	v_med3_f32 v8, v8, s66, v142
	v_med3_f32 v9, v9, s66, v142
	v_cvt_pk_fp8_f32 v5, v8, v9
	v_med3_f32 v10, v10, s66, v142
	v_med3_f32 v11, v11, s66, v142
	v_cvt_pk_fp8_f32 v5, v10, v11 op_sel:[0,0,1]
	global_store_dwordx2 v[6:7], v[4:5], off
	s_and_b64 vcc, exec, s[4:5]
	s_mov_b64 s[4:5], -1
	s_cbranch_vccnz .LBB0_1602
	s_andn2_b64 vcc, exec, s[10:11]
	s_cbranch_vccnz .LBB0_1601
	s_barrier
	s_branch .LBB0_1601
